# merge epilogue: the u8 merge gates are read exactly once, so their 32 load sites carry the nt (streaming) hint; plus previous changes
# baseline (speedup 1.0000x reference)
;     __device__ __forceinline__ void operator()(AccT& acc, const gm::GUnit& u, int wr, int wc, int fr, int fq) const {
;     ...
;         const unsigned char* gbase = G8 + (size_t)(u.pm * 256 + wr * 64 + fr) * INW + k * 1024 + u.pn * 256 + wc * 32 + 8 * fq;
; #pragma unroll
;         for (int q = 0; q < 4; ++q) {
;             const int ai = q >> 1, m0 = (q & 1) * 2;
;             u32x2 ga[2][2], gb[2][2];
; #pragma unroll
;             for (int mi = 0; mi < 2; ++mi)
; #pragma unroll
;                 for (int bj = 0; bj < 2; ++bj) {
;                     const unsigned char* gp = gbase + (size_t)(ai * 128 + (m0 + mi) * 16) * INW + bj * 128;
;                     ga[mi][bj] = *(const u32x2*)gp;
;                     gb[mi][bj] = (k < 3) ? *(const u32x2*)(gp + 1024) : (u32x2){0xffffffffu, 0xffffffffu};
;                 }
;             __builtin_amdgcn_sched_barrier(0);
; #pragma unroll
;             for (int mi = 0; mi < 2; ++mi) {
;                 const int m = m0 + mi, row = u.pm * 256 + ai * 128 + wr * 64 + m * 16 + fr;
; #pragma unroll
;                 for (int bj = 0; bj < 2; ++bj) {
;                     const u32x2 a = ga[mi][bj], b = gb[mi][bj];
;                     f32x4 r0, r1;
;                     r0[0] = (float)(a.x & 255u) * __builtin_amdgcn_rcpf((float)(b.x & 255u)); r0[1] = (float)((a.x >> 8) & 255u) * __builtin_amdgcn_rcpf((float)((b.x >> 8) & 255u));
;                     r0[2] = (float)((a.x >> 16) & 255u) * __builtin_amdgcn_rcpf((float)((b.x >> 16) & 255u)); r0[3] = (float)(a.x >> 24) * __builtin_amdgcn_rcpf((float)(b.x >> 24));
;                     r1[0] = (float)(a.y & 255u) * __builtin_amdgcn_rcpf((float)(b.y & 255u)); r1[1] = (float)((a.y >> 8) & 255u) * __builtin_amdgcn_rcpf((float)((b.y >> 8) & 255u));
;                     r1[2] = (float)((a.y >> 16) & 255u) * __builtin_amdgcn_rcpf((float)((b.y >> 16) & 255u)); r1[3] = (float)(a.y >> 24) * __builtin_amdgcn_rcpf((float)(b.y >> 24));
;                     const f32x4 s0 = acc[ai][bj][m][0] * r0, s1 = acc[ai][bj][m][1] * r1;
;                     if (k == 3) {
;                         u32x4 w; w.x = cvt_pk_bf16(s0[0], s0[1]); w.y = cvt_pk_bf16(s0[2], s0[3]); w.z = cvt_pk_bf16(s1[0], s1[1]); w.w = cvt_pk_bf16(s1[2], s1[3]);
;                         *(u32x4*)(M + (size_t)row * DM + u.pn * 256 + bj * 128 + wc * 32 + 8 * fq) = w;
;                     }
.LBB0_602:
	s_lshl_b32 s8, s28, 8
	v_mov_b32_e32 v136, v226
	v_mov_b32_e32 v130, v197
	s_add_i32 s8, s8, s91
	s_lshl_b32 s74, s42, 8
	v_add_u32_e32 v132, s8, v130
	v_ashrrev_i32_e32 v133, 31, v132
	v_lshlrev_b64 v[130:131], 12, v[132:133]
	s_lshl_b32 s8, s64, 10
	v_lshl_add_u64 v[130:131], s[46:47], 0, v[130:131]
	s_ashr_i32 s9, s8, 31
	v_lshl_add_u64 v[130:131], v[130:131], 0, s[8:9]
	s_ashr_i32 s75, s74, 31
	v_lshl_add_u64 v[130:131], v[130:131], 0, s[74:75]
	v_lshl_add_u64 v[134:135], v[130:131], 0, s[50:51]
	v_lshlrev_b32_e32 v130, 3, v136
	v_ashrrev_i32_e32 v131, 31, v130
	v_lshl_add_u64 v[134:135], v[134:135], 0, v[130:131]
	global_load_dwordx2 v[152:153], v[134:135], off nt
	s_cmp_lt_i32 s64, 3
	s_cselect_b64 s[8:9], -1, 0
	s_cmp_gt_i32 s64, 2
	v_mov_b32_e32 v144, -1
	v_mov_b32_e32 v154, -1
	v_mov_b32_e32 v155, -1
	s_cbranch_scc1 .LBB0_604
	global_load_dwordx2 v[154:155], v[134:135], off offset:1024 nt
.LBB0_604:
	global_load_dwordx2 v[148:149], v[134:135], off offset:128 nt
	v_cndmask_b32_e64 v136, 0, 1, s[8:9]
	v_cmp_ne_u32_e64 s[42:43], 1, v136
	s_andn2_b64 vcc, exec, s[8:9]
	v_mov_b32_e32 v145, -1
	s_cbranch_vccnz .LBB0_606
	global_load_dwordx2 v[144:145], v[134:135], off offset:1152 nt
.LBB0_606:
	v_add_co_u32_e32 v136, vcc, 0x10000, v134
	v_mov_b32_e32 v142, -1
	s_nop 0
	v_addc_co_u32_e32 v137, vcc, 0, v135, vcc
	global_load_dwordx2 v[140:141], v[136:137], off nt
	v_mov_b32_e32 v136, -1
	s_and_b64 vcc, exec, s[42:43]
	v_mov_b32_e32 v143, -1
	s_cbranch_vccnz .LBB0_608
	v_add_co_u32_e32 v138, vcc, 0x10000, v134
	s_nop 1
	v_addc_co_u32_e32 v139, vcc, 0, v135, vcc
	global_load_dwordx2 v[142:143], v[138:139], off offset:1024 nt
.LBB0_608:
	v_add_co_u32_e32 v138, vcc, 0x10000, v134
	v_mov_b32_e32 v137, -1
	s_nop 0
	v_addc_co_u32_e32 v139, vcc, 0, v135, vcc
	global_load_dwordx2 v[138:139], v[138:139], off offset:128 nt
	s_and_b64 vcc, exec, s[42:43]
	s_cbranch_vccnz .LBB0_610
	v_add_co_u32_e32 v136, vcc, 0x10000, v134
	s_nop 1
	v_addc_co_u32_e32 v137, vcc, 0, v135, vcc
	global_load_dwordx2 v[136:137], v[136:137], off offset:1152 nt
.LBB0_610:
	v_add_co_u32_e32 v234, vcc, 0x20000, v134
	s_nop 1
	v_addc_co_u32_e32 v235, vcc, 0, v135, vcc
	global_load_dwordx2 v[166:167], v[234:235], off nt
	global_load_dwordx2 v[168:169], v[234:235], off offset:1024 nt
	global_load_dwordx2 v[170:171], v[234:235], off offset:128 nt
	global_load_dwordx2 v[172:173], v[234:235], off offset:1152 nt
	v_add_co_u32_e32 v234, vcc, 0x30000, v134
	s_nop 1
	v_addc_co_u32_e32 v235, vcc, 0, v135, vcc
	global_load_dwordx2 v[174:175], v[234:235], off nt
	global_load_dwordx2 v[176:177], v[234:235], off offset:1024 nt
	global_load_dwordx2 v[178:179], v[234:235], off offset:128 nt
	global_load_dwordx2 v[192:193], v[234:235], off offset:1152 nt
	v_add_co_u32_e32 v234, vcc, 0x80000, v134
	s_nop 1
	v_addc_co_u32_e32 v235, vcc, 0, v135, vcc
	global_load_dwordx2 v[194:195], v[234:235], off nt
	global_load_dwordx2 v[200:201], v[234:235], off offset:1024 nt
	global_load_dwordx2 v[202:203], v[234:235], off offset:128 nt
	global_load_dwordx2 v[204:205], v[234:235], off offset:1152 nt
	v_add_co_u32_e32 v234, vcc, 0x90000, v134
	s_nop 1
	v_addc_co_u32_e32 v235, vcc, 0, v135, vcc
	global_load_dwordx2 v[206:207], v[234:235], off nt
	global_load_dwordx2 v[208:209], v[234:235], off offset:1024 nt
	global_load_dwordx2 v[210:211], v[234:235], off offset:128 nt
	global_load_dwordx2 v[224:225], v[234:235], off offset:1152 nt
	s_cmp_eq_u32 s64, 3
	s_cselect_b64 s[8:9], -1, 0
	s_cmp_lg_u32 s64, 3
	v_lshlrev_b64 v[150:151], 11, v[132:133]
	s_waitcnt vmcnt(16)
	v_cvt_f32_ubyte0_e32 v133, v154
	v_rcp_iflag_f32_e32 v156, v133
	v_cvt_f32_ubyte1_e32 v133, v154
	v_rcp_iflag_f32_e32 v157, v133
	v_cvt_f32_ubyte2_e32 v133, v154
	v_rcp_iflag_f32_e32 v158, v133
	v_cvt_f32_ubyte3_e32 v133, v154
	v_rcp_iflag_f32_e32 v159, v133
	v_cvt_f32_ubyte3_e32 v161, v152
	v_cvt_f32_ubyte2_e32 v160, v152
	v_cvt_f32_ubyte0_e32 v133, v155
	v_pk_mul_f32 v[158:159], v[158:159], v[160:161]
	v_rcp_iflag_f32_e32 v160, v133
	v_cvt_f32_ubyte1_e32 v133, v155
	v_rcp_iflag_f32_e32 v161, v133
	v_cvt_f32_ubyte2_e32 v133, v155
	v_rcp_iflag_f32_e32 v154, v133
	v_cvt_f32_ubyte3_e32 v133, v155
	v_rcp_iflag_f32_e32 v155, v133
	v_cvt_f32_ubyte1_e32 v163, v152
	v_cvt_f32_ubyte0_e32 v162, v152
	v_pk_mul_f32 v[156:157], v[156:157], v[162:163]
	v_cvt_f32_ubyte3_e32 v163, v153
	v_cvt_f32_ubyte2_e32 v162, v153
	v_cvt_f32_ubyte1_e32 v165, v153
	v_cvt_f32_ubyte0_e32 v164, v153
	v_pk_mul_f32 v[152:153], v[160:161], v[164:165]
	v_pk_mul_f32 v[154:155], v[154:155], v[162:163]
	v_pk_mul_f32 v[124:125], v[124:125], v[158:159]
	v_pk_mul_f32 v[122:123], v[122:123], v[156:157]
	v_pk_mul_f32 v[128:129], v[128:129], v[154:155]
	v_pk_mul_f32 v[126:127], v[126:127], v[152:153]
	s_mov_b32 s72, 1.0
	s_mov_b32 s70, 1.0
	s_cbranch_scc1 .LBB0_612
	v_lshl_add_u64 v[156:157], s[48:49], 0, v[150:151]
	v_lshl_add_u64 v[156:157], s[74:75], 1, v[156:157]
	s_lshl_b32 s76, s50, 1
	v_lshl_add_u64 v[156:157], v[156:157], 0, s[76:77]
	v_lshl_add_u64 v[156:157], v[130:131], 1, v[156:157]
	s_mov_b32 s70, 0
	v_cvt_pk_bf16_f32 v152, v122, v123
	v_cvt_pk_bf16_f32 v153, v124, v125
	v_cvt_pk_bf16_f32 v154, v126, v127
	v_cvt_pk_bf16_f32 v155, v128, v129
	global_store_dwordx4 v[156:157], v[152:155], off

;     __device__ __forceinline__ void operator()(AccT& acc, const gm::GUnit& u, int wr, int wc, int fr, int fq) const {
;     ...
;         for (int q = 0; q < 4; ++q) {
;             const int ai = q >> 1, m0 = (q & 1) * 2;
;             u32x2 ga[2][2], gb[2][2];
; #pragma unroll
;             for (int mi = 0; mi < 2; ++mi)
; #pragma unroll
;                 for (int bj = 0; bj < 2; ++bj) {
;                     const unsigned char* gp = gbase + (size_t)(ai * 128 + (m0 + mi) * 16) * INW + bj * 128;
;                     ga[mi][bj] = *(const u32x2*)gp;
;                     gb[mi][bj] = (k < 3) ? *(const u32x2*)(gp + 1024) : (u32x2){0xffffffffu, 0xffffffffu};
;                 }
;             __builtin_amdgcn_sched_barrier(0);
; #pragma unroll
;             for (int mi = 0; mi < 2; ++mi) {
;                 const int m = m0 + mi, row = u.pm * 256 + ai * 128 + wr * 64 + m * 16 + fr;
; #pragma unroll
;                 for (int bj = 0; bj < 2; ++bj) {
;                     const u32x2 a = ga[mi][bj], b = gb[mi][bj];
;                     f32x4 r0, r1;
;                     r0[0] = (float)(a.x & 255u) * __builtin_amdgcn_rcpf((float)(b.x & 255u)); r0[1] = (float)((a.x >> 8) & 255u) * __builtin_amdgcn_rcpf((float)((b.x >> 8) & 255u));
;                     r0[2] = (float)((a.x >> 16) & 255u) * __builtin_amdgcn_rcpf((float)((b.x >> 16) & 255u)); r0[3] = (float)(a.x >> 24) * __builtin_amdgcn_rcpf((float)(b.x >> 24));
;                     r1[0] = (float)(a.y & 255u) * __builtin_amdgcn_rcpf((float)(b.y & 255u)); r1[1] = (float)((a.y >> 8) & 255u) * __builtin_amdgcn_rcpf((float)((b.y >> 8) & 255u));
;                     r1[2] = (float)((a.y >> 16) & 255u) * __builtin_amdgcn_rcpf((float)((b.y >> 16) & 255u)); r1[3] = (float)(a.y >> 24) * __builtin_amdgcn_rcpf((float)(b.y >> 24));
;                     const f32x4 s0 = acc[ai][bj][m][0] * r0, s1 = acc[ai][bj][m][1] * r1;
;                     if (k == 3) {
;                         u32x4 w; w.x = cvt_pk_bf16(s0[0], s0[1]); w.y = cvt_pk_bf16(s0[2], s0[3]); w.z = cvt_pk_bf16(s1[0], s1[1]); w.w = cvt_pk_bf16(s1[2], s1[3]);
;                         *(u32x4*)(M + (size_t)row * DM + u.pn * 256 + bj * 128 + wc * 32 + 8 * fq) = w;
;                     }
;                     const float kz = (k == 3) ? 0.f : 1.f;
;                     acc[ai][bj][m][0] = s0 * kz; acc[ai][bj][m][1] = s1 * kz;
;                 }
.Lmg1_j:
	v_add_co_u32_e32 v234, vcc, 0xa0000, v134
	s_nop 1
	v_addc_co_u32_e32 v235, vcc, 0, v135, vcc
	global_load_dwordx2 v[166:167], v[234:235], off nt
	global_load_dwordx2 v[168:169], v[234:235], off offset:1024 nt
	global_load_dwordx2 v[170:171], v[234:235], off offset:128 nt
	global_load_dwordx2 v[172:173], v[234:235], off offset:1152 nt
	v_add_co_u32_e32 v234, vcc, 0xb0000, v134
	s_nop 1
	v_addc_co_u32_e32 v235, vcc, 0, v135, vcc
	global_load_dwordx2 v[174:175], v[234:235], off nt
	global_load_dwordx2 v[176:177], v[234:235], off offset:1024 nt
	global_load_dwordx2 v[178:179], v[234:235], off offset:128 nt
	global_load_dwordx2 v[192:193], v[234:235], off offset:1152 nt
	v_cvt_f32_ubyte0_e32 v133, v154
	v_rcp_iflag_f32_e32 v156, v133
	v_cvt_f32_ubyte1_e32 v133, v154
	v_rcp_iflag_f32_e32 v157, v133
	v_cvt_f32_ubyte2_e32 v133, v154
	v_rcp_iflag_f32_e32 v158, v133
	v_cvt_f32_ubyte3_e32 v133, v154
	v_rcp_iflag_f32_e32 v159, v133
	v_cvt_f32_ubyte3_e32 v161, v152
	v_cvt_f32_ubyte2_e32 v160, v152
	v_cvt_f32_ubyte0_e32 v133, v155
	v_pk_mul_f32 v[158:159], v[158:159], v[160:161]
	v_rcp_iflag_f32_e32 v160, v133
	v_cvt_f32_ubyte1_e32 v133, v155
	v_rcp_iflag_f32_e32 v161, v133
	v_cvt_f32_ubyte2_e32 v133, v155
	v_rcp_iflag_f32_e32 v154, v133
	v_cvt_f32_ubyte3_e32 v133, v155
	v_rcp_iflag_f32_e32 v155, v133
	v_cvt_f32_ubyte1_e32 v163, v152
	v_cvt_f32_ubyte0_e32 v162, v152
	v_add_u32_e32 v150, 32, v132
	v_pk_mul_f32 v[156:157], v[156:157], v[162:163]
	v_cvt_f32_ubyte3_e32 v163, v153
	v_cvt_f32_ubyte2_e32 v162, v153
	v_cvt_f32_ubyte1_e32 v165, v153
	v_cvt_f32_ubyte0_e32 v164, v153
	v_ashrrev_i32_e32 v151, 31, v150
	v_pk_mul_f32 v[152:153], v[160:161], v[164:165]
	v_pk_mul_f32 v[154:155], v[154:155], v[162:163]
	v_lshlrev_b64 v[150:151], 11, v[150:151]
	v_pk_mul_f32 v[92:93], v[92:93], v[158:159]
	v_pk_mul_f32 v[90:91], v[90:91], v[156:157]
	v_pk_mul_f32 v[96:97], v[96:97], v[154:155]
	v_pk_mul_f32 v[94:95], v[94:95], v[152:153]
	s_mov_b32 s84, 1.0
	s_and_b64 vcc, exec, s[40:41]
	s_mov_b32 s82, 1.0
	s_cbranch_vccnz .LBB0_628
	v_lshl_add_u64 v[156:157], s[48:49], 0, v[150:151]
	v_lshl_add_u64 v[156:157], s[74:75], 1, v[156:157]
	s_lshl_b32 s76, s50, 1
	v_lshl_add_u64 v[156:157], v[156:157], 0, s[76:77]
	v_lshl_add_u64 v[156:157], v[130:131], 1, v[156:157]
	s_mov_b32 s82, 0
	v_cvt_pk_bf16_f32 v152, v90, v91
	v_cvt_pk_bf16_f32 v153, v92, v93
	v_cvt_pk_bf16_f32 v154, v94, v95
	v_cvt_pk_bf16_f32 v155, v96, v97
	global_store_dwordx4 v[156:157], v[152:155], off
